# baseline (speedup 1.0000x reference)
.LBB5_15:
	s_or_b64 exec, exec, s[6:7]
	s_load_dwordx4 s[4:7], s[0:1], 0x18
	v_mov_b32_e32 v17, 0
	s_waitcnt lgkmcnt(0)
	s_barrier
	ds_read_b32 v17, v17 offset:32776
	s_and_b32 s17, s5, 0xffff
	s_and_b32 s21, s15, 0xffff
	v_accvgpr_read_b32 v56, a0
	v_lshlrev_b32_e32 v15, 12, v1
	v_lshlrev_b32_e32 v18, 4, v56
	s_add_u32 s8, s4, s7
	s_mov_b32 s16, s4
	v_lshlrev_b32_e32 v14, 14, v10
	v_lshlrev_b32_e32 v16, 7, v0
	s_addc_u32 s9, s5, 0
	s_waitcnt lgkmcnt(0)
	v_cmp_ne_u32_e64 s[4:5], 0, v17
	v_add_u32_e32 v17, 0, v15
	v_or_b32_e32 v15, v18, v15
	v_or3_b32 v15, v16, v14, v15
	v_lshlrev_b32_e32 v13, 3, v0
	v_accvgpr_write_b32 a98, v15
	v_and_b32_e32 v15, 63, v57
	v_lshlrev_b32_e32 v19, 4, v13
	v_lshrrev_b32_e32 v15, 5, v15
	s_waitcnt vmcnt(1)
	v_mul_f32_e32 v45, 0xbfb8aa3b, v6
	v_mul_f32_e32 v6, 0xbfb8aa3b, v7
	v_mul_f32_e32 v7, 0xbfb8aa3b, v9
	v_lshlrev_b32_e32 v9, 8, v1
	v_add3_u32 v17, v17, v19, v18
	v_accvgpr_write_b32 a94, v15
	v_bfe_u32 v16, v57, 2, 3
	v_lshlrev_b32_e32 v15, 3, v57
	v_add_u32_e32 v9, v23, v9
	v_accvgpr_write_b32 a97, v17
	v_and_b32_e32 v17, 24, v15
	v_lshlrev_b32_e32 v10, 13, v10
	v_lshlrev_b32_e32 v15, 10, v16
	v_or_b32_e32 v9, v9, v13
	v_or3_b32 v10, v10, v15, v17
	v_cmp_eq_u32_e64 s[2:3], 3, v1
	v_lshl_add_u32 v9, v9, 1, s6
	v_accvgpr_write_b32 a95, v16
	v_lshl_add_u32 v16, v10, 1, s44
	v_lshlrev_b32_e32 v1, 7, v1
	v_and_b32_e32 v10, 8, v57
	v_lshlrev_b32_e32 v0, 1, v0
	v_or3_b32 v1, v1, v10, v0
	v_add_u32_e32 v10, s24, v9
	s_lshl_b32 s6, s33, 9
	v_or3_b32 v1, v1, v18, v14
	v_accvgpr_write_b32 a99, v10
	v_add_u32_e32 v10, s26, v9
	v_add_u32_e32 v1, s6, v1
	s_and_b32 s33, s6, 0xe00
	s_lshl_b32 s6, s42, 9
	v_accvgpr_write_b32 a102, v10
	v_add_u32_e32 v10, s28, v9
	s_and_b32 s35, s6, 0xe00
	s_lshl_b32 s6, s43, 9
	v_accvgpr_write_b32 a103, v10
	v_add_u32_e32 v10, s30, v9
	s_and_b32 s37, s6, 0xe00
	s_lshl_b32 s6, s45, 9
	v_accvgpr_write_b32 a104, v10
	v_add_u32_e32 v10, s34, v9
	v_accvgpr_write_b32 a96, v17
	v_ashrrev_i32_e32 v17, 31, v16
	s_and_b32 s39, s6, 0xe00
	s_lshl_b32 s6, s46, 9
	v_accvgpr_write_b32 a105, v10
	v_add_u32_e32 v10, s36, v9
	v_accvgpr_write_b32 a93, v17
	s_and_b32 s41, s6, 0xe00
	s_lshl_b32 s6, s47, 9
	v_accvgpr_write_b32 a106, v10
	v_add_u32_e32 v10, s38, v9
	v_add_u32_e32 v9, s40, v9
	v_or_b32_e32 v13, v13, v56
	v_accvgpr_write_b32 a92, v16
	v_lshl_add_u64 v[16:17], s[8:9], 0, v[16:17]
	s_and_b32 s42, s6, 0xe00
	s_lshl_b32 s6, s48, 9
	v_accvgpr_write_b32 a108, v9
	v_lshlrev_b32_e32 v9, 1, v12
	s_mov_b32 s19, 0x20000
	v_accvgpr_write_b32 a101, v17
	s_and_b32 s43, s6, 0xe00
	s_lshl_b32 s6, s49, 9
	v_accvgpr_write_b32 a107, v10
	v_add3_u32 v0, 0, v9, v0
	v_lshlrev_b32_e32 v9, 9, v11
	v_lshlrev_b32_e32 v10, 4, v13
	s_brev_b32 s18, -2
	s_mov_b32 s22, 0x80000
	s_mov_b32 s23, s19
	s_mov_b32 s20, s14
	v_cmp_gt_u32_e64 s[0:1], 8, v22
	s_mov_b32 s15, 0
	v_accvgpr_write_b32 a100, v16
	s_and_b32 s44, s6, 0xe00
	v_add3_u32 v9, 0, v9, v10
	s_mov_b64 s[26:27], 0
	s_mov_b32 s34, 0x80008000
	s_mov_b32 s36, 0x100000
	s_brev_b32 s38, 60
	s_mov_b32 s40, 0xbc38aa3b
	s_mov_b32 s45, 0x41000000
	s_waitcnt vmcnt(0)
	v_accvgpr_write_b32 a112, v250
	v_accvgpr_write_b32 a113, v251
	v_accvgpr_write_b32 a114, v252
	v_accvgpr_write_b32 a115, v253
	v_accvgpr_write_b32 a116, v2
	v_accvgpr_write_b32 a117, v3
	v_accvgpr_write_b32 a118, v4
	v_accvgpr_write_b32 a119, v5
	v_and_b32_e32 v46, 2, v57
	v_cmp_ne_u32_e64 s[0:1], 0, v46
	v_and_b32_e32 v46, 32, v57
	v_cmp_ne_u32_e64 s[30:31], 0, v46
	v_mov_b32_e32 v26, 0x44444444
	v_mov_b32_e32 v46, 0xeeeeeeee
	v_cndmask_b32_e64 v26, v26, v46, s[0:1]
	v_accvgpr_read_b32 v46, a98
	v_bfe_u32 v47, v57, 4, 2
	v_lshlrev_b32_e32 v47, 7, v47
	v_sub_u32_e32 v46, v46, v47
	v_and_b32_e32 v47, 7, v57
	v_lshlrev_b32_e32 v47, 4, v47
	v_sub_u32_e32 v46, v46, v47
	v_bfe_u32 v47, v57, 4, 1
	v_lshl_add_u32 v46, v47, 8, v46
	v_and_b32_e32 v47, 15, v57
	v_lshl_add_u32 v46, v47, 4, v46
	v_mov_b32_e32 v47, s33
	v_mov_b32_e32 v48, s35
	v_cndmask_b32_e64 v47, v47, v48, s[30:31]
	v_or_b32_e32 v27, v46, v47
	v_mov_b32_e32 v47, s37
	v_mov_b32_e32 v48, s39
	v_cndmask_b32_e64 v47, v47, v48, s[30:31]
	v_or_b32_e32 v28, v46, v47
	v_mov_b32_e32 v47, s41
	v_mov_b32_e32 v48, s42
	v_cndmask_b32_e64 v47, v47, v48, s[30:31]
	v_or_b32_e32 v29, v46, v47
	v_mov_b32_e32 v47, s43
	v_mov_b32_e32 v48, s44
	v_cndmask_b32_e64 v47, v47, v48, s[30:31]
	v_or_b32_e32 v30, v46, v47
	v_lshrrev_b32_e32 v46, 6, v57
	v_lshlrev_b32_e32 v46, 7, v46
	v_and_b32_e32 v47, 8, v57
	v_bfe_u32 v48, v57, 4, 2
	v_lshl_or_b32 v47, v48, 1, v47
	v_add_u32_e32 v46, v46, v47
	v_and_b32_e32 v47, 7, v57
	v_lshl_add_u32 v46, v47, 4, v46
	v_sub_u32_e32 v1, v1, v46
	v_bfe_u32 v46, v57, 7, 1
	v_lshlrev_b32_e32 v46, 8, v46
	v_bfe_u32 v47, v57, 1, 2
	v_lshl_or_b32 v46, v47, 6, v46
	v_bfe_u32 v47, v57, 5, 1
	v_lshl_or_b32 v46, v47, 5, v46
	v_and_b32_e32 v47, 1, v57
	v_lshl_or_b32 v46, v47, 4, v46
	v_bfe_u32 v47, v57, 3, 1
	v_bfe_u32 v48, v57, 6, 1
	v_lshl_or_b32 v47, v48, 1, v47
	v_lshl_or_b32 v46, v47, 2, v46
	v_bfe_u32 v47, v57, 4, 1
	v_lshl_or_b32 v46, v47, 1, v46
	v_add_u32_e32 v1, v1, v46
	v_lshrrev_b32_e32 v46, 6, v57
	v_lshlrev_b32_e32 v46, 12, v46
	v_bfe_u32 v47, v57, 4, 2
	v_lshl_or_b32 v46, v47, 10, v46
	v_and_b32_e32 v47, 3, v57
	v_lshl_or_b32 v46, v47, 2, v46
	v_bfe_u32 v47, v57, 3, 1
	v_bfe_u32 v48, v57, 4, 1
	v_xor_b32_e32 v47, v47, v48
	v_lshl_or_b32 v46, v47, 5, v46
	v_bfe_u32 v47, v57, 5, 1
	v_lshl_or_b32 v46, v47, 7, v46
	v_bfe_u32 v47, v57, 2, 1
	v_lshl_or_b32 v31, v47, 4, v46
	v_xor_b32_e32 v32, 0x80, v31
	v_xor_b32_e32 v47, 1, v47
	v_lshl_or_b32 v33, v47, 4, v46
	v_add_u32_e32 v33, 0x200, v33
	v_xor_b32_e32 v34, 0x80, v33
	v_lshrrev_b32_e32 v46, 3, v57
	v_and_b32_e32 v46, 24, v46
	v_lshrrev_b32_e32 v47, 1, v57
	v_and_or_b32 v46, v47, 4, v46
	v_bfe_u32 v47, v57, 4, 2
	v_or_b32_e32 v46, v46, v47
	v_and_b32_e32 v47, 3, v57
	v_and_b32_e32 v48, 4, v57
	v_lshl_or_b32 v47, v48, 1, v47
	v_xor_b32_e32 v46, v46, v47
	v_and_b32_e32 v47, 7, v57
	v_lshlrev_b32_e32 v47, 9, v47
	v_lshl_or_b32 v9, v46, 4, v47
	v_accvgpr_write_b32 a120, v226
	v_accvgpr_write_b32 a121, v227
	v_accvgpr_write_b32 a122, v228
	v_accvgpr_write_b32 a123, v229
	v_accvgpr_write_b32 a124, v230
	v_accvgpr_write_b32 a125, v231
	v_accvgpr_write_b32 a126, v232
	v_accvgpr_write_b32 a127, v233
	v_accvgpr_write_b32 a128, v234
	v_accvgpr_write_b32 a129, v235
	v_accvgpr_write_b32 a130, v236
	v_accvgpr_write_b32 a131, v237
	v_accvgpr_write_b32 a132, v238
	v_accvgpr_write_b32 a133, v239
	v_accvgpr_write_b32 a134, v240
	v_accvgpr_write_b32 a135, v241
	v_accvgpr_write_b32 a136, v242
	v_accvgpr_write_b32 a137, v243
	v_accvgpr_write_b32 a138, v244
	v_accvgpr_write_b32 a139, v245
	v_accvgpr_write_b32 a140, v246
	v_accvgpr_write_b32 a141, v247
	v_accvgpr_write_b32 a142, v248
	v_accvgpr_write_b32 a143, v249
	v_accvgpr_write_b32 a144, v194
	v_accvgpr_write_b32 a145, v195
	v_accvgpr_write_b32 a146, v196
	v_accvgpr_write_b32 a147, v197
	v_accvgpr_write_b32 a148, v198
	v_accvgpr_write_b32 a149, v199
	v_accvgpr_write_b32 a150, v200
	v_accvgpr_write_b32 a151, v201
	v_accvgpr_write_b32 a152, v202
	v_accvgpr_write_b32 a153, v203
	v_accvgpr_write_b32 a154, v204
	v_accvgpr_write_b32 a155, v205
	v_accvgpr_write_b32 a156, v206
	v_accvgpr_write_b32 a157, v207
	v_accvgpr_write_b32 a158, v208
	v_accvgpr_write_b32 a159, v209
	v_accvgpr_write_b32 a160, v210
	v_accvgpr_write_b32 a161, v211
	v_accvgpr_write_b32 a162, v212
	v_accvgpr_write_b32 a163, v213
	v_accvgpr_write_b32 a164, v214
	v_accvgpr_write_b32 a165, v215
	v_accvgpr_write_b32 a166, v216
	v_accvgpr_write_b32 a167, v217
	v_accvgpr_write_b32 a168, v218
	v_accvgpr_write_b32 a169, v219
	v_accvgpr_write_b32 a170, v220
	v_accvgpr_write_b32 a171, v221
	v_accvgpr_write_b32 a172, v222
	v_accvgpr_write_b32 a173, v223
	v_accvgpr_write_b32 a174, v224
	v_accvgpr_write_b32 a175, v225
	s_mov_b64 s[24:25], 0
	s_mov_b32 s46, 0
	s_mov_b32 s30, 0x3c38aa3b
	s_mov_b32 s31, 0xbc000000
	v_mov_b32_e32 v35, 0
	s_mov_b32 s49, 8
	s_mov_b32 s50, 0
	v_bfe_u32 v50, v57, 4, 2
	v_lshlrev_b32_e32 v50, 4, v50
	v_bfe_u32 v51, v57, 4, 1
	v_bfe_u32 v52, v57, 1, 1
	v_lshlrev_b32_e32 v52, 2, v52
	v_lshl_or_b32 v51, v51, 5, v52
	v_sub_u32_e32 v54, v51, v50
	v_bfe_u32 v51, v57, 2, 2
	v_and_b32_e32 v52, 1, v57
	v_lshl_or_b32 v51, v51, 1, v52
	v_and_b32_e32 v52, 7, v57
	v_sub_u32_e32 v51, v51, v52
	v_lshlrev_b32_e32 v51, 11, v51
	v_add_u32_e32 v54, v54, v51
	v_and_b32_e32 v55, 32, v57
	v_cmp_ne_u32_e64 s[28:29], 0, v55
	v_accvgpr_read_b32 v242, a99
	v_accvgpr_read_b32 v55, a102
	v_cndmask_b32_e64 v242, v242, v55, s[28:29]
	v_add_u32_e32 v242, v242, v54
	v_accvgpr_read_b32 v243, a103
	v_accvgpr_read_b32 v55, a104
	v_cndmask_b32_e64 v243, v243, v55, s[28:29]
	v_add_u32_e32 v243, v243, v54
	v_accvgpr_read_b32 v244, a105
	v_accvgpr_read_b32 v55, a106
	v_cndmask_b32_e64 v244, v244, v55, s[28:29]
	v_add_u32_e32 v244, v244, v54
	v_accvgpr_read_b32 v245, a107
	v_accvgpr_read_b32 v55, a108
	v_cndmask_b32_e64 v245, v245, v55, s[28:29]
	v_add_u32_e32 v245, v245, v54
	s_mov_b64 s[26:27], -1
	v_mov_b32_e32 v10, 0
	v_mov_b32_e32 v11, 0
	v_mov_b32_e32 v12, 0
	v_mov_b32_e32 v13, 0
	v_mov_b32_e32 v14, 0
	v_mov_b32_e32 v15, 0
	v_mov_b32_e32 v16, 0
	v_mov_b32_e32 v17, 0
	v_mov_b32_e32 v18, 0
	v_mov_b32_e32 v19, 0
	v_mov_b32_e32 v20, 0
	v_mov_b32_e32 v21, 0
	v_mov_b32_e32 v22, 0
	v_mov_b32_e32 v23, 0
	v_mov_b32_e32 v24, 0
	v_mov_b32_e32 v25, 0
	v_mov_b32_e32 v2, 0
	v_mov_b32_e32 v3, 0
	v_mov_b32_e32 v4, 0
	v_mov_b32_e32 v5, 0
	v_mov_b32_e32 v250, 0
	v_mov_b32_e32 v251, 0
	v_mov_b32_e32 v252, 0
	v_mov_b32_e32 v253, 0
	v_mov_b32_e32 v46, 0
	v_mov_b32_e32 v47, 0
	v_mov_b32_e32 v48, 0
	v_mov_b32_e32 v49, 0
	v_mov_b32_e32 v50, 0
	v_mov_b32_e32 v51, 0
	v_mov_b32_e32 v52, 0
	v_mov_b32_e32 v53, 0
	buffer_load_dword v226, v242, s[16:19], 0 offen sc1
	buffer_load_dword v227, v242, s[16:19], 0 offen offset:8 sc1
	buffer_load_dword v228, v242, s[16:19], 0 offen offset:16 sc1
	buffer_load_dword v229, v242, s[16:19], 0 offen offset:24 sc1
	buffer_load_dword v230, v243, s[16:19], 0 offen sc1
	buffer_load_dword v231, v243, s[16:19], 0 offen offset:8 sc1
	buffer_load_dword v232, v243, s[16:19], 0 offen offset:16 sc1
	buffer_load_dword v233, v243, s[16:19], 0 offen offset:24 sc1
	buffer_load_dword v234, v244, s[16:19], 0 offen sc1
	buffer_load_dword v235, v244, s[16:19], 0 offen offset:8 sc1
	buffer_load_dword v236, v244, s[16:19], 0 offen offset:16 sc1
	buffer_load_dword v237, v244, s[16:19], 0 offen offset:24 sc1
	buffer_load_dword v238, v245, s[16:19], 0 offen sc1
	buffer_load_dword v239, v245, s[16:19], 0 offen offset:8 sc1
	buffer_load_dword v240, v245, s[16:19], 0 offen offset:16 sc1
	buffer_load_dword v241, v245, s[16:19], 0 offen offset:24 sc1
	s_waitcnt vmcnt(0)

.Lrec_c0:
	v_bitop3_b32 v54, v194, v195, s28 bitop3:0x7e
	v_bitop3_b32 v55, v196, v197, s28 bitop3:0x7e
	v_bitop3_b32 v54, v54, v55, s34 bitop3:0xa8
	v_cmp_ne_u32_e32 vcc, 0, v54
	s_andn2_b64 vcc, vcc, s[26:27]
	s_cbranch_vccnz .Lrec_retry0
	v_smfmac_f32_16x16x64_f16 v[10:13], v[194:197], a[36:43], v26
	v_smfmac_f32_16x16x64_f16 v[14:17], v[194:197], a[68:75], v26
	v_smfmac_f32_16x16x64_f16 v[18:21], v[194:197], v[66:73], v26
	v_smfmac_f32_16x16x64_f16 v[22:25], v[194:197], v[98:105], v26
	v_smfmac_f32_16x16x64_f16 v[46:49], v[194:197], v[130:137], v26
	v_smfmac_f32_16x16x64_f16 v[50:53], v[194:197], v[162:169], v26
	v_smfmac_f32_16x16x64_f16 v[2:5], v[194:197], a[144:151], v26
	v_smfmac_f32_16x16x64_f16 v[250:253], v[194:197], a[120:127], v26

.Lrec_c1:
	v_bitop3_b32 v54, v198, v199, s28 bitop3:0x7e
	v_bitop3_b32 v55, v200, v201, s28 bitop3:0x7e
	v_bitop3_b32 v54, v54, v55, s34 bitop3:0xa8
	v_cmp_ne_u32_e32 vcc, 0, v54
	s_andn2_b64 vcc, vcc, s[26:27]
	s_cbranch_vccnz .Lrec_retry1
	v_smfmac_f32_16x16x64_f16 v[10:13], v[198:201], a[44:51], v26
	v_smfmac_f32_16x16x64_f16 v[14:17], v[198:201], a[76:83], v26
	v_smfmac_f32_16x16x64_f16 v[18:21], v[198:201], v[74:81], v26
	v_smfmac_f32_16x16x64_f16 v[22:25], v[198:201], v[106:113], v26
	v_smfmac_f32_16x16x64_f16 v[46:49], v[198:201], v[138:145], v26
	v_smfmac_f32_16x16x64_f16 v[50:53], v[198:201], v[170:177], v26
	v_smfmac_f32_16x16x64_f16 v[2:5], v[198:201], a[152:159], v26
	v_smfmac_f32_16x16x64_f16 v[250:253], v[198:201], a[128:135], v26

.Lrec_c2:
	v_bitop3_b32 v54, v202, v203, s28 bitop3:0x7e
	v_bitop3_b32 v55, v204, v205, s28 bitop3:0x7e
	v_bitop3_b32 v54, v54, v55, s34 bitop3:0xa8
	v_cmp_ne_u32_e32 vcc, 0, v54
	s_andn2_b64 vcc, vcc, s[26:27]
	s_cbranch_vccnz .Lrec_retry2
	v_smfmac_f32_16x16x64_f16 v[10:13], v[202:205], a[52:59], v26
	v_smfmac_f32_16x16x64_f16 v[14:17], v[202:205], a[84:91], v26
	v_smfmac_f32_16x16x64_f16 v[18:21], v[202:205], v[82:89], v26
	v_smfmac_f32_16x16x64_f16 v[22:25], v[202:205], v[114:121], v26
	v_smfmac_f32_16x16x64_f16 v[46:49], v[202:205], v[146:153], v26
	v_smfmac_f32_16x16x64_f16 v[50:53], v[202:205], v[178:185], v26
	v_smfmac_f32_16x16x64_f16 v[2:5], v[202:205], a[160:167], v26
	v_smfmac_f32_16x16x64_f16 v[250:253], v[202:205], a[136:143], v26

.Lrec_c3:
	v_bitop3_b32 v54, v206, v207, s28 bitop3:0x7e
	v_bitop3_b32 v55, v208, v209, s28 bitop3:0x7e
	v_bitop3_b32 v54, v54, v55, s34 bitop3:0xa8
	v_cmp_ne_u32_e32 vcc, 0, v54
	s_andn2_b64 vcc, vcc, s[26:27]
	s_cbranch_vccnz .Lrec_retry3
	v_smfmac_f32_16x16x64_f16 v[10:13], v[206:209], a[60:67], v26
	v_smfmac_f32_16x16x64_f16 v[14:17], v[206:209], v[58:65], v26
	v_smfmac_f32_16x16x64_f16 v[18:21], v[206:209], v[90:97], v26
	v_smfmac_f32_16x16x64_f16 v[22:25], v[206:209], v[122:129], v26
	v_smfmac_f32_16x16x64_f16 v[46:49], v[206:209], v[154:161], v26
	v_smfmac_f32_16x16x64_f16 v[50:53], v[206:209], v[186:193], v26
	v_smfmac_f32_16x16x64_f16 v[2:5], v[206:209], a[168:175], v26
	v_smfmac_f32_16x16x64_f16 v[250:253], v[206:209], a[112:119], v26

.Lrec_stored:
	s_cmpk_eq_i32 s14, 0x100
	s_cbranch_scc1 .Lrec_exit
	v_and_or_b32 v15, s29, 56, v56
	v_lshl_add_u32 v15, v15, 6, v0
	ds_write_b16 v15, v14 offset:33024
	v_mov_b32_e32 v44, v12
	v_add_u32_e32 v242, s7, v27
	v_add_u32_e32 v243, s7, v28
	v_add_u32_e32 v244, s7, v29
	v_add_u32_e32 v245, s7, v30
	v_xor_b32_e32 v31, 0x4000, v31
	v_xor_b32_e32 v32, 0x4000, v32
	v_xor_b32_e32 v33, 0x4000, v33
	v_xor_b32_e32 v34, 0x4000, v34
	v_xor_b32_e32 v9, 0x4000, v9
	v_mov_b32_e32 v10, 0
	v_mov_b32_e32 v11, 0
	v_mov_b32_e32 v12, 0
	v_mov_b32_e32 v13, 0
	v_mov_b32_e32 v14, 0
	v_mov_b32_e32 v15, 0
	v_mov_b32_e32 v16, 0
	v_mov_b32_e32 v17, 0
	v_mov_b32_e32 v18, 0
	v_mov_b32_e32 v19, 0
	v_mov_b32_e32 v20, 0
	v_mov_b32_e32 v21, 0
	v_mov_b32_e32 v22, 0
	v_mov_b32_e32 v23, 0
	v_mov_b32_e32 v24, 0
	v_mov_b32_e32 v25, 0
	v_mov_b32_e32 v2, 0
	v_mov_b32_e32 v3, 0
	v_mov_b32_e32 v4, 0
	v_mov_b32_e32 v5, 0
	v_mov_b32_e32 v250, 0
	v_mov_b32_e32 v251, 0
	v_mov_b32_e32 v252, 0
	v_mov_b32_e32 v253, 0
	s_mov_b64 s[26:27], s[24:25]
	v_mov_b32_e32 v46, 0
	v_mov_b32_e32 v47, 0
	v_mov_b32_e32 v48, 0
	v_mov_b32_e32 v49, 0
	v_mov_b32_e32 v50, 0
	v_mov_b32_e32 v51, 0
	v_mov_b32_e32 v52, 0
	v_mov_b32_e32 v53, 0
	s_and_b32 s29, s46, 1
	s_cmp_eq_u32 s29, 0
	s_cselect_b32 s29, -1, 0
	s_cmp_lg_u32 s50, 0
	s_cselect_b32 s29, 1, s29
	s_add_i32 s49, s49, s29
	s_max_i32 s49, s49, 0
	s_min_i32 s49, s49, 30
	s_mov_b32 s50, 0
	s_mov_b32 s29, s49
.Lrec_dl:
	s_nop 15
	s_sub_u32 s29, s29, 1
	s_cmp_gt_i32 s29, 0
	s_cbranch_scc1 .Lrec_dl
	buffer_load_dwordx4 v[194:197], v242, s[20:23], 0 offen sc1
	buffer_load_dwordx4 v[198:201], v243, s[20:23], 0 offen sc1
	buffer_load_dwordx4 v[202:205], v244, s[20:23], 0 offen sc1
	buffer_load_dwordx4 v[206:209], v245, s[20:23], 0 offen sc1
	s_cmp_eq_u64 s[2:3], 0
	s_cbranch_scc1 .Lrec_noflush
	s_and_b32 s29, s46, 3
	s_cmp_lg_u32 s29, 0
	s_cbranch_scc1 .Lrec_noflush
	s_cmp_lt_u32 s46, 4
	s_cbranch_scc1 .Lrec_noflush
	s_add_i32 s29, s46, -4
	v_accvgpr_read_b32 v46, a94
	v_or_b32_e32 v50, s29, v46
	v_lshlrev_b32_e32 v46, 3, v50
	v_accvgpr_read_b32 v47, a95
	v_and_or_b32 v46, v46, 40, v47
	v_accvgpr_read_b32 v47, a96
	v_lshl_add_u32 v47, v47, 1, 0
	v_lshl_add_u32 v54, v46, 6, v47
	ds_read_b128 v[46:49], v54 offset:33024
	v_ashrrev_i32_e32 v51, 31, v50
	v_accvgpr_read_b32 v52, a100
	v_lshlrev_b64 v[50:51], 17, v[50:51]
	v_accvgpr_read_b32 v53, a101
	v_lshl_add_u64 v[50:51], v[52:53], 0, v[50:51]
	v_add_co_u32_e32 v52, vcc, 0x20000, v50
	s_nop 1
	v_addc_co_u32_e32 v53, vcc, 0, v51, vcc
	s_waitcnt lgkmcnt(0)
	global_store_dwordx4 v[52:53], v[46:49], off
	s_nop 1
	ds_read_b128 v[46:49], v54 offset:34048
	v_add_co_u32_e32 v50, vcc, 0x60000, v50
	s_nop 1
	v_addc_co_u32_e32 v51, vcc, 0, v51, vcc
	s_waitcnt lgkmcnt(0)
	global_store_dwordx4 v[50:51], v[46:49], off
	s_nop 1
	v_mov_b32_e32 v46, 0
	v_mov_b32_e32 v47, 0
	v_mov_b32_e32 v48, 0
	v_mov_b32_e32 v49, 0
	v_mov_b32_e32 v50, 0
	v_mov_b32_e32 v51, 0
	v_mov_b32_e32 v52, 0
	v_mov_b32_e32 v53, 0

.Lrec_retry0:
	s_mov_b32 s50, 1
	s_add_i32 s14, s14, 1
	s_cmp_gt_u32 s14, 0x40000
	s_cbranch_scc1 .Lrec_dead0
	buffer_load_dwordx4 v[194:197], v242, s[20:23], 0 offen sc1
	buffer_load_dwordx4 v[198:201], v243, s[20:23], 0 offen sc1
	buffer_load_dwordx4 v[202:205], v244, s[20:23], 0 offen sc1
	buffer_load_dwordx4 v[206:209], v245, s[20:23], 0 offen sc1
	s_branch .Lrec_b0

.Lrec_retry1:
	s_mov_b32 s50, 1
	s_add_i32 s14, s14, 1
	s_cmp_gt_u32 s14, 0x40000
	s_cbranch_scc1 .Lrec_dead1
	buffer_load_dwordx4 v[198:201], v243, s[20:23], 0 offen sc1
	buffer_load_dwordx4 v[202:205], v244, s[20:23], 0 offen sc1
	buffer_load_dwordx4 v[206:209], v245, s[20:23], 0 offen sc1
	s_branch .Lrec_b1

.Lrec_retry2:
	s_mov_b32 s50, 1
	s_add_i32 s14, s14, 1
	s_cmp_gt_u32 s14, 0x40000
	s_cbranch_scc1 .Lrec_dead2
	buffer_load_dwordx4 v[202:205], v244, s[20:23], 0 offen sc1
	buffer_load_dwordx4 v[206:209], v245, s[20:23], 0 offen sc1
	s_branch .Lrec_b2

.Lrec_retry3:
	s_mov_b32 s50, 1
	s_add_i32 s14, s14, 1
	s_cmp_gt_u32 s14, 0x40000
	s_cbranch_scc1 .Lrec_dead3
	buffer_load_dwordx4 v[206:209], v245, s[20:23], 0 offen sc1
	s_branch .Lrec_b3

	.amdhsa_kernel _Z5k_recPKDF16_S0_PKfS0_jjS2_PfS3_PDF16_Pj
		.amdhsa_group_segment_fixed_size 0
		.amdhsa_private_segment_fixed_size 0
		.amdhsa_kernarg_size 80
		.amdhsa_user_sgpr_count 2
		.amdhsa_user_sgpr_dispatch_ptr 0
		.amdhsa_user_sgpr_queue_ptr 0
		.amdhsa_user_sgpr_kernarg_segment_ptr 1
		.amdhsa_user_sgpr_dispatch_id 0
		.amdhsa_user_sgpr_kernarg_preload_length 0
		.amdhsa_user_sgpr_kernarg_preload_offset 0
		.amdhsa_user_sgpr_private_segment_size 0
		.amdhsa_uses_dynamic_stack 0
		.amdhsa_enable_private_segment 0
		.amdhsa_system_sgpr_workgroup_id_x 1
		.amdhsa_system_sgpr_workgroup_id_y 0
		.amdhsa_system_sgpr_workgroup_id_z 0
		.amdhsa_system_sgpr_workgroup_info 0
		.amdhsa_system_vgpr_workitem_id 0
		.amdhsa_next_free_vgpr 432
		.amdhsa_next_free_sgpr 52
		.amdhsa_accum_offset 256
		.amdhsa_reserve_vcc 1
		.amdhsa_float_round_mode_32 0
		.amdhsa_float_round_mode_16_64 0
		.amdhsa_float_denorm_mode_32 3
		.amdhsa_float_denorm_mode_16_64 3
		.amdhsa_dx10_clamp 1
		.amdhsa_ieee_mode 1
		.amdhsa_fp16_overflow 0
		.amdhsa_tg_split 0
		.amdhsa_exception_fp_ieee_invalid_op 0
		.amdhsa_exception_fp_denorm_src 0
		.amdhsa_exception_fp_ieee_div_zero 0
		.amdhsa_exception_fp_ieee_overflow 0
		.amdhsa_exception_fp_ieee_underflow 0
		.amdhsa_exception_fp_ieee_inexact 0
		.amdhsa_exception_int_div_zero 0
	.end_amdhsa_kernel

amdhsa.kernels:
  - .agpr_count:     0
    .args:
      - .offset:         0
        .size:           288
        .value_kind:     by_value
    .group_segment_fixed_size: 16640
    .kernarg_segment_align: 8
    .kernarg_segment_size: 288
    .language:       OpenCL C
    .language_version:
      - 2
      - 0
    .max_flat_workgroup_size: 1024
    .name:           _Z8k_wt_all6WtJobs
    .private_segment_fixed_size: 0
    .sgpr_count:     30
    .sgpr_spill_count: 0
    .symbol:         _Z8k_wt_all6WtJobs.kd
    .uniform_work_group_size: 1
    .uses_dynamic_stack: false
    .vgpr_count:     44
    .vgpr_spill_count: 0
    .wavefront_size: 64
  - .agpr_count:     0
    .args:
      - .actual_access:  read_only
        .address_space:  global
        .offset:         0
        .size:           8
        .value_kind:     global_buffer
      - .actual_access:  read_only
        .address_space:  global
        .offset:         8
        .size:           8
        .value_kind:     global_buffer
      - .actual_access:  write_only
        .address_space:  global
        .offset:         16
        .size:           8
        .value_kind:     global_buffer
    .group_segment_fixed_size: 0
    .kernarg_segment_align: 8
    .kernarg_segment_size: 24
    .language:       OpenCL C
    .language_version:
      - 2
      - 0
    .max_flat_workgroup_size: 1024
    .name:           _Z8k_prepA1PKfS0_PDF16_
    .private_segment_fixed_size: 0
    .sgpr_count:     16
    .sgpr_spill_count: 0
    .symbol:         _Z8k_prepA1PKfS0_PDF16_.kd
    .uniform_work_group_size: 1
    .uses_dynamic_stack: false
    .vgpr_count:     15
    .vgpr_spill_count: 0
    .wavefront_size: 64
  - .agpr_count:     0
    .args:
      - .actual_access:  read_only
        .address_space:  global
        .offset:         0
        .size:           8
        .value_kind:     global_buffer
      - .actual_access:  read_only
        .address_space:  global
        .offset:         8
        .size:           8
        .value_kind:     global_buffer
      - .actual_access:  read_only
        .address_space:  global
        .offset:         16
        .size:           8
        .value_kind:     global_buffer
      - .actual_access:  write_only
        .address_space:  global
        .offset:         24
        .size:           8
        .value_kind:     global_buffer
    .group_segment_fixed_size: 4096
    .kernarg_segment_align: 8
    .kernarg_segment_size: 32
    .language:       OpenCL C
    .language_version:
      - 2
      - 0
    .max_flat_workgroup_size: 1024
    .name:           _Z7k_bias0PKfPKiS0_Pf
    .private_segment_fixed_size: 0
    .sgpr_count:     28
    .sgpr_spill_count: 0
    .symbol:         _Z7k_bias0PKfPKiS0_Pf.kd
    .uniform_work_group_size: 1
    .uses_dynamic_stack: false
    .vgpr_count:     78
    .vgpr_spill_count: 0
    .wavefront_size: 64
  - .agpr_count:     0
    .args:
      - .actual_access:  read_only
        .address_space:  global
        .offset:         0
        .size:           8
        .value_kind:     global_buffer
      - .actual_access:  read_only
        .address_space:  global
        .offset:         8
        .size:           8
        .value_kind:     global_buffer
      - .actual_access:  read_only
        .address_space:  global
        .offset:         16
        .size:           8
        .value_kind:     global_buffer
      - .actual_access:  read_only
        .address_space:  global
        .offset:         24
        .size:           8
        .value_kind:     global_buffer
      - .actual_access:  read_only
        .address_space:  global
        .offset:         32
        .size:           8
        .value_kind:     global_buffer
      - .actual_access:  write_only
        .address_space:  global
        .offset:         40
        .size:           8
        .value_kind:     global_buffer
    .group_segment_fixed_size: 0
    .kernarg_segment_align: 8
    .kernarg_segment_size: 48
    .language:       OpenCL C
    .language_version:
      - 2
      - 0
    .max_flat_workgroup_size: 1024
    .name:           _Z7k_biasLPKfS0_S0_S0_S0_Pf
    .private_segment_fixed_size: 0
    .sgpr_count:     24
    .sgpr_spill_count: 0
    .symbol:         _Z7k_biasLPKfS0_S0_S0_S0_Pf.kd
    .uniform_work_group_size: 1
    .uses_dynamic_stack: false
    .vgpr_count:     29
    .vgpr_spill_count: 0
    .wavefront_size: 64
  - .agpr_count:     0
    .args:
      - .actual_access:  read_only
        .address_space:  global
        .offset:         0
        .size:           8
        .value_kind:     global_buffer
      - .actual_access:  read_only
        .address_space:  global
        .offset:         8
        .size:           8
        .value_kind:     global_buffer
      - .actual_access:  write_only
        .address_space:  global
        .offset:         16
        .size:           8
        .value_kind:     global_buffer
      - .actual_access:  write_only
        .address_space:  global
        .offset:         24
        .size:           8
        .value_kind:     global_buffer
    .group_segment_fixed_size: 0
    .kernarg_segment_align: 8
    .kernarg_segment_size: 32
    .language:       OpenCL C
    .language_version:
      - 2
      - 0
    .max_flat_workgroup_size: 1024
    .name:           _Z8k_state0PKfS0_PDF16_Pf
    .private_segment_fixed_size: 0
    .sgpr_count:     18
    .sgpr_spill_count: 0
    .symbol:         _Z8k_state0PKfS0_PDF16_Pf.kd
    .uniform_work_group_size: 1
    .uses_dynamic_stack: false
    .vgpr_count:     7
    .vgpr_spill_count: 0
    .wavefront_size: 64
  - .agpr_count:     176
    .args:
      - .actual_access:  read_only
        .address_space:  global
        .offset:         0
        .size:           8
        .value_kind:     global_buffer
      - .actual_access:  read_only
        .address_space:  global
        .offset:         8
        .size:           8
        .value_kind:     global_buffer
      - .actual_access:  read_only
        .address_space:  global
        .offset:         16
        .size:           8
        .value_kind:     global_buffer
      - .address_space:  global
        .offset:         24
        .size:           8
        .value_kind:     global_buffer
      - .offset:         32
        .size:           4
        .value_kind:     by_value
      - .offset:         36
        .size:           4
        .value_kind:     by_value
      - .address_space:  global
        .offset:         40
        .size:           8
        .value_kind:     global_buffer
      - .address_space:  global
        .offset:         48
        .size:           8
        .value_kind:     global_buffer
      - .address_space:  global
        .offset:         56
        .size:           8
        .value_kind:     global_buffer
      - .address_space:  global
        .offset:         64
        .size:           8
        .value_kind:     global_buffer
      - .address_space:  global
        .offset:         72
        .size:           8
        .value_kind:     global_buffer
    .group_segment_fixed_size: 0
    .kernarg_segment_align: 8
    .kernarg_segment_size: 80
    .language:       OpenCL C
    .language_version:
      - 2
      - 0
    .max_flat_workgroup_size: 256
    .name:           _Z5k_recPKDF16_S0_PKfS0_jjS2_PfS3_PDF16_Pj
    .private_segment_fixed_size: 0
    .sgpr_count:     58
    .sgpr_spill_count: 0
    .symbol:         _Z5k_recPKDF16_S0_PKfS0_jjS2_PfS3_PDF16_Pj.kd
    .uniform_work_group_size: 1
    .uses_dynamic_stack: false
    .vgpr_count:     432
    .vgpr_spill_count: 0
    .wavefront_size: 64
  - .agpr_count:     0
    .args:
      - .address_space:  global
        .offset:         0
        .size:           8
        .value_kind:     global_buffer
    .group_segment_fixed_size: 0
    .kernarg_segment_align: 8
    .kernarg_segment_size: 8
    .language:       OpenCL C
    .language_version:
      - 2
      - 0
    .max_flat_workgroup_size: 1024
    .name:           _Z9k_softmaxPf
    .private_segment_fixed_size: 0
    .sgpr_count:     9
    .sgpr_spill_count: 0
    .symbol:         _Z9k_softmaxPf.kd
    .uniform_work_group_size: 1
    .uses_dynamic_stack: false
    .vgpr_count:     32
    .vgpr_spill_count: 0
    .wavefront_size: 64
  - .agpr_count:     0
    .args:
      - .address_space:  global
        .offset:         0
        .size:           8
        .value_kind:     global_buffer
      - .address_space:  global
        .offset:         8
        .size:           8
        .value_kind:     global_buffer
      - .actual_access:  write_only
        .address_space:  global
        .offset:         16
        .size:           8
        .value_kind:     global_buffer
      - .actual_access:  read_only
        .address_space:  global
        .offset:         24
        .size:           8
        .value_kind:     global_buffer
    .group_segment_fixed_size: 0
    .kernarg_segment_align: 8
    .kernarg_segment_size: 32
    .language:       OpenCL C
    .language_version:
      - 2
      - 0
    .max_flat_workgroup_size: 512
    .name:           _Z6k_gemmILi16384ELi4096ELi2048ELi0EEvPKDF16_S1_PvPKf
    .private_segment_fixed_size: 0
    .sgpr_count:     25
    .sgpr_spill_count: 0
    .symbol:         _Z6k_gemmILi16384ELi4096ELi2048ELi0EEvPKDF16_S1_PvPKf.kd
    .uniform_work_group_size: 1
    .uses_dynamic_stack: false
    .vgpr_count:     244
    .vgpr_spill_count: 0
    .wavefront_size: 64
  - .agpr_count:     0
    .args:
      - .address_space:  global
        .offset:         0
        .size:           8
        .value_kind:     global_buffer
      - .address_space:  global
        .offset:         8
        .size:           8
        .value_kind:     global_buffer
      - .actual_access:  write_only
        .address_space:  global
        .offset:         16
        .size:           8
        .value_kind:     global_buffer
      - .actual_access:  read_only
        .address_space:  global
        .offset:         24
        .size:           8
        .value_kind:     global_buffer
    .group_segment_fixed_size: 0
    .kernarg_segment_align: 8
    .kernarg_segment_size: 32
    .language:       OpenCL C
    .language_version:
      - 2
      - 0
    .max_flat_workgroup_size: 512
    .name:           _Z6k_gemmILi16384ELi4096ELi1024ELi0EEvPKDF16_S1_PvPKf
    .private_segment_fixed_size: 0
    .sgpr_count:     26
    .sgpr_spill_count: 0
    .symbol:         _Z6k_gemmILi16384ELi4096ELi1024ELi0EEvPKDF16_S1_PvPKf.kd
    .uniform_work_group_size: 1
    .uses_dynamic_stack: false
    .vgpr_count:     244
    .vgpr_spill_count: 0
    .wavefront_size: 64
  - .agpr_count:     0
    .args:
      - .address_space:  global
        .offset:         0
        .size:           8
        .value_kind:     global_buffer
      - .address_space:  global
        .offset:         8
        .size:           8
        .value_kind:     global_buffer
      - .actual_access:  write_only
        .address_space:  global
        .offset:         16
        .size:           8
        .value_kind:     global_buffer
      - .actual_access:  read_only
        .address_space:  global
        .offset:         24
        .size:           8
        .value_kind:     global_buffer
    .group_segment_fixed_size: 0
    .kernarg_segment_align: 8
    .kernarg_segment_size: 32
    .language:       OpenCL C
    .language_version:
      - 2
      - 0
    .max_flat_workgroup_size: 512
    .name:           _Z6k_gemmILi16384ELi1024ELi1024ELi1EEvPKDF16_S1_PvPKf
    .private_segment_fixed_size: 0
    .sgpr_count:     28
    .sgpr_spill_count: 0
    .symbol:         _Z6k_gemmILi16384ELi1024ELi1024ELi1EEvPKDF16_S1_PvPKf.kd
    .uniform_work_group_size: 1
    .uses_dynamic_stack: false
    .vgpr_count:     246
    .vgpr_spill_count: 0
    .wavefront_size: 64
